# speedup vs baseline: 1.0143x; 1.0143x over previous
.LBB1_30:
	s_or_b64 exec, exec, s[2:3]
	v_lshlrev_b32_e32 v4, 2, v16
	ds_read_b128 v[0:3], v4
	ds_read_b128 v[16:19], v4 offset:16
	ds_read_b128 v[20:23], v4 offset:512
	v_cmp_eq_u32_e64 s[2:3], 0, v24
	s_and_b64 s[2:3], s[2:3], vcc
	s_waitcnt lgkmcnt(2)
	v_pk_fma_f32 v[30:31], v[6:7], v[0:1], 0 op_sel_hi:[0,1,0]
	v_pk_fma_f32 v[54:55], v[6:7], v[2:3], 0 op_sel_hi:[0,1,0]
	ds_read_b128 v[26:29], v4 offset:1024
	ds_read_b128 v[0:3], v4 offset:528
	s_waitcnt lgkmcnt(3)
	v_pk_fma_f32 v[16:17], v[6:7], v[16:17], 0 op_sel_hi:[0,1,0]
	v_pk_fma_f32 v[6:7], v[6:7], v[18:19], 0 op_sel_hi:[0,1,0]
	s_waitcnt lgkmcnt(2)
	v_pk_fma_f32 v[34:35], v[14:15], v[20:21], v[30:31] op_sel_hi:[0,1,1]
	ds_read_b128 v[18:21], v4 offset:1536
	ds_read_b128 v[30:33], v4 offset:1040
	s_waitcnt lgkmcnt(3)
	v_pk_fma_f32 v[26:27], v[14:15], v[26:27], v[34:35] op_sel:[1,0,0]
	ds_read_b128 v[34:37], v4 offset:2048
	ds_read_b128 v[38:41], v4 offset:2560
	ds_read_b128 v[42:45], v4 offset:1552
	ds_read_b128 v[46:49], v4 offset:2064
	ds_read_b128 v[50:53], v4 offset:2576
	v_pk_fma_f32 v[22:23], v[14:15], v[22:23], v[54:55] op_sel_hi:[0,1,1]
	v_pk_fma_f32 v[22:23], v[14:15], v[28:29], v[22:23] op_sel:[1,0,0]
	s_waitcnt lgkmcnt(6)
	v_pk_fma_f32 v[18:19], v[12:13], v[18:19], v[26:27] op_sel_hi:[0,1,1]
	ds_read_b128 v[54:57], v4 offset:3072
	ds_read_b128 v[58:61], v4 offset:3088
	v_pk_fma_f32 v[20:21], v[12:13], v[20:21], v[22:23] op_sel_hi:[0,1,1]
	v_pk_fma_f32 v[0:1], v[14:15], v[0:1], v[16:17] op_sel_hi:[0,1,1]
	v_pk_fma_f32 v[2:3], v[14:15], v[2:3], v[6:7] op_sel_hi:[0,1,1]
	s_waitcnt lgkmcnt(6)
	v_pk_fma_f32 v[18:19], v[12:13], v[34:35], v[18:19] op_sel:[1,0,0]
	ds_read_b128 v[26:29], v4 offset:3584
	v_pk_fma_f32 v[20:21], v[12:13], v[36:37], v[20:21] op_sel:[1,0,0]
	ds_read_b128 v[34:37], v4 offset:3600
	v_pk_fma_f32 v[0:1], v[14:15], v[30:31], v[0:1] op_sel:[1,0,0]
	v_pk_fma_f32 v[2:3], v[14:15], v[32:33], v[2:3] op_sel:[1,0,0]
	s_waitcnt lgkmcnt(6)
	v_pk_fma_f32 v[0:1], v[12:13], v[42:43], v[0:1] op_sel_hi:[0,1,1]
	v_pk_fma_f32 v[2:3], v[12:13], v[44:45], v[2:3] op_sel_hi:[0,1,1]
	s_waitcnt lgkmcnt(5)
	v_pk_fma_f32 v[0:1], v[12:13], v[46:47], v[0:1] op_sel:[1,0,0]
	v_pk_fma_f32 v[2:3], v[12:13], v[48:49], v[2:3] op_sel:[1,0,0]
	v_pk_fma_f32 v[18:19], v[8:9], v[38:39], v[18:19] op_sel_hi:[0,1,1]
	v_pk_fma_f32 v[20:21], v[8:9], v[40:41], v[20:21] op_sel_hi:[0,1,1]
	s_waitcnt lgkmcnt(4)
	v_pk_fma_f32 v[0:1], v[8:9], v[50:51], v[0:1] op_sel_hi:[0,1,1]
	v_pk_fma_f32 v[2:3], v[8:9], v[52:53], v[2:3] op_sel_hi:[0,1,1]
	s_waitcnt lgkmcnt(3)
	v_pk_fma_f32 v[18:19], v[8:9], v[54:55], v[18:19] op_sel:[1,0,0]
	v_mov_b32_e32 v38, v5
	v_pk_fma_f32 v[20:21], v[8:9], v[56:57], v[20:21] op_sel:[1,0,0]
	s_waitcnt lgkmcnt(2)
	v_pk_fma_f32 v[0:1], v[8:9], v[58:59], v[0:1] op_sel:[1,0,0]
	v_pk_fma_f32 v[2:3], v[8:9], v[60:61], v[2:3] op_sel:[1,0,0]
	s_waitcnt lgkmcnt(1)
	v_pk_fma_f32 v[4:5], v[38:39], v[26:27], v[18:19] op_sel_hi:[0,1,1]
	v_pk_fma_f32 v[20:21], v[38:39], v[28:29], v[20:21] op_sel_hi:[0,1,1]
	s_waitcnt lgkmcnt(0)
	v_pk_fma_f32 v[0:1], v[38:39], v[34:35], v[0:1] op_sel_hi:[0,1,1]
	v_pk_fma_f32 v[2:3], v[38:39], v[36:37], v[2:3] op_sel_hi:[0,1,1]
	v_add_f32_dpp v4, v4, v4 quad_perm:[1,0,3,2] row_mask:0xf bank_mask:0xf
	v_add_f32_dpp v5, v5, v5 quad_perm:[1,0,3,2] row_mask:0xf bank_mask:0xf
	v_add_f32_dpp v20, v20, v20 quad_perm:[1,0,3,2] row_mask:0xf bank_mask:0xf
	v_add_f32_dpp v21, v21, v21 quad_perm:[1,0,3,2] row_mask:0xf bank_mask:0xf
	v_add_f32_dpp v0, v0, v0 quad_perm:[1,0,3,2] row_mask:0xf bank_mask:0xf
	v_add_f32_dpp v1, v1, v1 quad_perm:[1,0,3,2] row_mask:0xf bank_mask:0xf
	v_add_f32_dpp v2, v2, v2 quad_perm:[1,0,3,2] row_mask:0xf bank_mask:0xf
	v_add_f32_dpp v3, v3, v3 quad_perm:[1,0,3,2] row_mask:0xf bank_mask:0xf
	v_add_f32_dpp v4, v4, v4 quad_perm:[2,3,0,1] row_mask:0xf bank_mask:0xf
	v_add_f32_dpp v5, v5, v5 quad_perm:[2,3,0,1] row_mask:0xf bank_mask:0xf
	v_add_f32_dpp v20, v20, v20 quad_perm:[2,3,0,1] row_mask:0xf bank_mask:0xf
	v_add_f32_dpp v21, v21, v21 quad_perm:[2,3,0,1] row_mask:0xf bank_mask:0xf
	v_add_f32_dpp v0, v0, v0 quad_perm:[2,3,0,1] row_mask:0xf bank_mask:0xf
	v_add_f32_dpp v1, v1, v1 quad_perm:[2,3,0,1] row_mask:0xf bank_mask:0xf
	v_add_f32_dpp v2, v2, v2 quad_perm:[2,3,0,1] row_mask:0xf bank_mask:0xf
	v_add_f32_dpp v3, v3, v3 quad_perm:[2,3,0,1] row_mask:0xf bank_mask:0xf
	v_add_f32_dpp v4, v4, v4 row_half_mirror row_mask:0xf bank_mask:0xf
	v_add_f32_dpp v5, v5, v5 row_half_mirror row_mask:0xf bank_mask:0xf
	v_add_f32_dpp v20, v20, v20 row_half_mirror row_mask:0xf bank_mask:0xf
	v_add_f32_dpp v21, v21, v21 row_half_mirror row_mask:0xf bank_mask:0xf
	v_add_f32_dpp v0, v0, v0 row_half_mirror row_mask:0xf bank_mask:0xf
	v_add_f32_dpp v1, v1, v1 row_half_mirror row_mask:0xf bank_mask:0xf
	v_add_f32_dpp v2, v2, v2 row_half_mirror row_mask:0xf bank_mask:0xf
	v_add_f32_dpp v3, v3, v3 row_half_mirror row_mask:0xf bank_mask:0xf
	v_lshlrev_b32_e32 v24, 2, v10
	v_ashrrev_i32_e32 v25, 31, v24
	v_lshlrev_b64 v[24:25], 2, v[24:25]
	v_add_f32_dpp v8, v4, v4 row_mirror row_mask:0xf bank_mask:0xf
	v_add_f32_dpp v9, v5, v5 row_mirror row_mask:0xf bank_mask:0xf
	v_add_f32_dpp v10, v20, v20 row_mirror row_mask:0xf bank_mask:0xf
	v_add_f32_dpp v11, v21, v21 row_mirror row_mask:0xf bank_mask:0xf
	v_add_f32_dpp v0, v0, v0 row_mirror row_mask:0xf bank_mask:0xf
	v_add_f32_dpp v1, v1, v1 row_mirror row_mask:0xf bank_mask:0xf
	v_add_f32_dpp v2, v2, v2 row_mirror row_mask:0xf bank_mask:0xf
	v_add_f32_dpp v3, v3, v3 row_mirror row_mask:0xf bank_mask:0xf
	s_and_saveexec_b64 s[4:5], s[2:3]
	s_cbranch_execz .LBB1_32
	s_load_dwordx4 s[0:3], s[0:1], 0x38
	s_waitcnt lgkmcnt(0)
	v_lshl_add_u64 v[26:27], s[0:1], 0, v[24:25]
	v_lshl_add_u64 v[24:25], s[2:3], 0, v[24:25]
	global_store_dwordx4 v[26:27], v[8:11], off
	global_store_dwordx4 v[24:25], v[0:3], off
